# speedup vs baseline: 1.0476x; 1.0476x over previous
_Z9gemm_gldsILi256ELi192ELi4ELi2ELi2ELi4ELi8ELi0ELi4096ELi3072ELi1024EEvPKDF16_S1_PfPKfS4_PKiPDF16_S7_S7_:
	s_ashr_i32 s3, s2, 3
	s_lshr_b32 s9, s3, 30
	s_add_i32 s9, s3, s9
	s_lshl_b32 s8, s2, 1
	s_ashr_i32 s10, s9, 2
	s_and_b32 s9, s9, 0xfffffc
	s_lshl_b32 s2, s2, 3
	s_load_dwordx4 s[4:7], s[0:1], 0x0
	s_and_b32 s8, s8, 12
	s_sub_i32 s3, s3, s9
	s_and_b32 s20, s2, 8
	s_add_i32 s8, s8, s3
	s_add_i32 s20, s20, s10
	s_lshl_b32 s16, s8, 8
	s_mul_i32 s2, s20, 0xc0
	v_lshlrev_b32_e32 v139, 4, v0
	v_and_b32_e32 v1, 32, v0
	s_ashr_i32 s17, s16, 31
	s_ashr_i32 s3, s2, 31
	v_lshrrev_b32_e32 v2, 3, v0
	v_bfe_u32 v46, v0, 2, 4
	v_bitop3_b32 v1, v139, v1, 48 bitop3:0x6c
	s_lshl_b64 s[8:9], s[16:17], 11
	s_lshl_b64 s[10:11], s[2:3], 11
	v_and_or_b32 v2, v2, 48, v46
	v_and_or_b32 v47, v0, 64, v1
	s_waitcnt lgkmcnt(0)
	s_add_u32 s2, s4, s8
	s_addc_u32 s3, s5, s9
	v_lshrrev_b32_e32 v2, 3, v0
	v_and_b32_e32 v47, 7, v2
	v_and_b32_e32 v46, 7, v0
	v_xor_b32_e32 v47, v46, v47
	v_lshlrev_b32_e32 v47, 4, v47
	v_lshl_or_b32 v2, v2, 11, v47
	v_add_u32_e32 v194, 0x100, v2
	v_mov_b32_e32 v3, 0
	v_readfirstlane_b32 s4, v139
	v_or_b32_e32 v1, 0x2000, v139
	s_add_u32 s18, s6, s10
	v_lshl_add_u64 v[4:5], s[2:3], 0, v[2:3]
	s_mov_b32 m0, s4
	s_mov_b64 s[4:5], 0x20000
	v_readfirstlane_b32 s6, v1
	v_or_b32_e32 v1, 0x4000, v139
	s_addc_u32 s19, s7, s11
	v_readfirstlane_b32 s45, v139
	s_mov_b64 s[24:25], s[2:3]
	s_add_u32 s26, s2, 0x20000
	s_addc_u32 s27, s3, 0
	s_add_u32 s28, s2, 0x40000
	s_addc_u32 s29, s3, 0
	s_add_u32 s30, s2, 0x60000
	s_addc_u32 s31, s3, 0
	s_mov_b64 s[32:33], s[18:19]
	s_add_u32 s34, s18, 0x20000
	s_addc_u32 s35, s19, 0
	s_add_u32 s36, s18, 0x40000
	s_addc_u32 s37, s19, 0
	global_load_lds_dwordx4 v2, s[2:3]
	v_lshl_add_u64 v[8:9], v[4:5], 0, s[4:5]
	s_mov_b32 m0, s6
	s_mov_b64 s[6:7], 0x40000
	v_readfirstlane_b32 s8, v1
	global_load_lds_dwordx4 v[8:9], off
	v_lshl_add_u64 v[8:9], v[4:5], 0, s[6:7]
	s_mov_b32 m0, s8
	s_mov_b64 s[8:9], 0x60000
	v_or_b32_e32 v1, 0x6000, v139
	global_load_lds_dwordx4 v[8:9], off
	v_lshl_add_u64 v[8:9], v[4:5], 0, s[8:9]
	v_readfirstlane_b32 s8, v1
	v_or_b32_e32 v1, 0x8000, v139
	v_lshl_add_u64 v[6:7], s[18:19], 0, v[2:3]
	s_mov_b32 m0, s8
	v_readfirstlane_b32 s8, v1
	v_or_b32_e32 v1, 0xa000, v139
	global_load_lds_dwordx4 v[8:9], off
	s_mov_b32 m0, s8
	v_lshl_add_u64 v[8:9], v[6:7], 0, s[4:5]
	v_readfirstlane_b32 s4, v1
	v_or_b32_e32 v1, 0xc000, v139
	global_load_lds_dwordx4 v2, s[18:19]
	s_mov_b32 m0, s4
	v_readfirstlane_b32 s4, v1
	v_or_b32_e32 v1, 0xe000, v139
	global_load_lds_dwordx4 v[8:9], off
	v_lshl_add_u64 v[8:9], v[6:7], 0, s[6:7]
	s_mov_b32 m0, s4
	s_mov_b64 s[4:5], 0x80
	v_readfirstlane_b32 s6, v1
	v_or_b32_e32 v1, 0x10000, v139
	global_load_lds_dwordx4 v[8:9], off
	v_lshl_add_u64 v[8:9], v[4:5], 0, s[4:5]
	s_mov_b32 m0, s6
	s_mov_b64 s[6:7], 0x20080
	v_readfirstlane_b32 s8, v1
	v_or_b32_e32 v1, 0x12000, v139
	global_load_lds_dwordx4 v[8:9], off
	v_lshl_add_u64 v[8:9], v[4:5], 0, s[6:7]
	s_mov_b32 m0, s8
	v_readfirstlane_b32 s10, v1
	global_load_lds_dwordx4 v[8:9], off
	s_mov_b64 s[8:9], 0x40080
	s_mov_b32 m0, s10
	s_mov_b64 s[10:11], 0x60080
	v_or_b32_e32 v1, 0x14000, v139
	v_lshl_add_u64 v[8:9], v[4:5], 0, s[8:9]
	v_lshl_add_u64 v[4:5], v[4:5], 0, s[10:11]
	v_readfirstlane_b32 s10, v1
	global_load_lds_dwordx4 v[8:9], off
	s_mov_b32 m0, s10
	v_or_b32_e32 v1, 0x16000, v139
	global_load_lds_dwordx4 v[4:5], off
	v_lshl_add_u64 v[4:5], v[6:7], 0, s[4:5]
	v_readfirstlane_b32 s4, v1
	v_or_b32_e32 v1, 0x18000, v139
	s_mov_b32 m0, s4
	v_readfirstlane_b32 s4, v1
	v_or_b32_e32 v1, 0x1a000, v139
	global_load_lds_dwordx4 v[4:5], off
	v_lshl_add_u64 v[4:5], v[6:7], 0, s[6:7]
	s_mov_b32 m0, s4
	v_readfirstlane_b32 s4, v1
	global_load_lds_dwordx4 v[4:5], off
	v_lshl_add_u64 v[4:5], v[6:7], 0, s[8:9]
	s_mov_b32 m0, s4
	v_lshrrev_b32_e32 v2, 7, v0
	global_load_lds_dwordx4 v[4:5], off
	s_load_dwordx4 s[12:15], s[0:1], 0x38
	s_load_dwordx8 s[4:11], s[0:1], 0x18
	v_lshlrev_b32_e32 v4, 6, v0
	v_and_b32_e32 v138, 48, v0
	v_and_b32_e32 v4, 0x3c0, v4
	v_lshlrev_b32_e32 v6, 2, v0
	v_bfe_u32 v144, v0, 6, 1
	v_or_b32_e32 v14, v4, v138
	v_lshlrev_b32_e32 v5, 13, v2
	v_and_b32_e32 v15, 32, v6
	v_and_b32_e32 v1, 15, v0
	v_and_b32_e32 v14, 15, v0
	v_bfe_u32 v15, v0, 4, 2
	v_and_b32_e32 v6, 7, v14
	v_xor_b32_e32 v15, v15, v6
	v_lshlrev_b32_e32 v15, 4, v15
	v_lshl_or_b32 v14, v14, 7, v15
	v_mov_b32_e32 v15, 0
	v_mov_b32_e32 v151, v14
	v_bitop3_b32 v146, v5, v14, v15 bitop3:0xf6
	v_mul_u32_u24_e32 v152, 0x3000, v144
	v_lshl_or_b32 v145, v2, 6, s16
	v_or_b32_e32 v4, v145, v1
	v_ashrrev_i32_e32 v5, 31, v4
	s_waitcnt lgkmcnt(0)
	v_lshl_add_u64 v[4:5], v[4:5], 2, s[8:9]
	global_load_dword v150, v[4:5], off
	global_load_dword v149, v[4:5], off offset:64
	global_load_dword v148, v[4:5], off offset:128
	global_load_dword v147, v[4:5], off offset:192
	v_bitop3_b32 v153, v152, v14, v15 bitop3:0xf6
	v_xor_b32_e32 v214, 64, v146
	v_xor_b32_e32 v215, 64, v153
	v_mov_b32_e32 v48, v3
	v_mov_b32_e32 v49, v3
	v_mov_b32_e32 v50, v3
	v_mov_b32_e32 v51, v3
	v_mov_b32_e32 v52, v3
	v_mov_b32_e32 v53, v3
	v_mov_b32_e32 v54, v3
	v_mov_b32_e32 v55, v3
	v_mov_b32_e32 v56, v3
	v_mov_b32_e32 v57, v3
	v_mov_b32_e32 v58, v3
	v_mov_b32_e32 v59, v3
	v_mov_b32_e32 v60, v3
	v_mov_b32_e32 v61, v3
	v_mov_b32_e32 v62, v3
	v_mov_b32_e32 v63, v3
	v_mov_b32_e32 v64, v3
	v_mov_b32_e32 v65, v3
	v_mov_b32_e32 v66, v3
	v_mov_b32_e32 v67, v3
	v_mov_b32_e32 v68, v3
	v_mov_b32_e32 v69, v3
	v_mov_b32_e32 v70, v3
	v_mov_b32_e32 v71, v3
	v_mov_b32_e32 v72, v3
	v_mov_b32_e32 v73, v3
	v_mov_b32_e32 v74, v3
	v_mov_b32_e32 v75, v3
	v_mov_b32_e32 v76, v3
	v_mov_b32_e32 v77, v3
	v_mov_b32_e32 v86, v3
	v_mov_b32_e32 v87, v3
	v_mov_b32_e32 v88, v3
	v_mov_b32_e32 v89, v3
	v_mov_b32_e32 v98, v3
	v_mov_b32_e32 v99, v3
	v_mov_b32_e32 v100, v3
	v_mov_b32_e32 v101, v3
	v_mov_b32_e32 v130, v3
	v_mov_b32_e32 v131, v3
	v_mov_b32_e32 v132, v3
	v_mov_b32_e32 v133, v3
	v_mov_b32_e32 v78, v3
	v_mov_b32_e32 v79, v3
	v_mov_b32_e32 v80, v3
	v_mov_b32_e32 v81, v3
	v_mov_b32_e32 v82, v3
	v_mov_b32_e32 v83, v3
	v_mov_b32_e32 v84, v3
	v_mov_b32_e32 v85, v3
	v_mov_b32_e32 v90, v3
	v_mov_b32_e32 v91, v3
	v_mov_b32_e32 v92, v3
	v_mov_b32_e32 v93, v3
	v_mov_b32_e32 v94, v3
	v_mov_b32_e32 v95, v3
	v_mov_b32_e32 v96, v3
	v_mov_b32_e32 v97, v3
	v_mov_b32_e32 v102, v3
	v_mov_b32_e32 v103, v3
	v_mov_b32_e32 v104, v3
	v_mov_b32_e32 v105, v3
	v_mov_b32_e32 v106, v3
	v_mov_b32_e32 v107, v3
	v_mov_b32_e32 v108, v3
	v_mov_b32_e32 v109, v3
	v_mov_b32_e32 v110, v3
	v_mov_b32_e32 v111, v3
	v_mov_b32_e32 v112, v3
	v_mov_b32_e32 v113, v3
	v_mov_b32_e32 v114, v3
	v_mov_b32_e32 v115, v3
	v_mov_b32_e32 v116, v3
	v_mov_b32_e32 v117, v3
	v_mov_b32_e32 v118, v3
	v_mov_b32_e32 v119, v3
	v_mov_b32_e32 v120, v3
	v_mov_b32_e32 v121, v3
	v_mov_b32_e32 v122, v3
	v_mov_b32_e32 v123, v3
	v_mov_b32_e32 v124, v3
	v_mov_b32_e32 v125, v3
	v_mov_b32_e32 v134, v3
	v_mov_b32_e32 v135, v3
	v_mov_b32_e32 v136, v3
	v_mov_b32_e32 v137, v3
	v_mov_b32_e32 v126, v3
	v_mov_b32_e32 v127, v3
	v_mov_b32_e32 v128, v3
	v_mov_b32_e32 v129, v3
	s_waitcnt vmcnt(7) lgkmcnt(0)
	s_barrier
	ds_read_b128 v[42:45], v146
	ds_read_b128 v[38:41], v146 offset:2048
	ds_read_b128 v[10:13], v146 offset:4096
	ds_read_b128 v[6:9], v146 offset:6144
	ds_read_b128 v[22:25], v153 offset:32768
	ds_read_b128 v[18:21], v153 offset:34816
	ds_read_b128 v[30:33], v153 offset:36864
	ds_read_b128 v[26:29], v153 offset:38912
	ds_read_b128 v[34:37], v153 offset:40960
	ds_read_b128 v[14:17], v153 offset:43008
	v_lshl_or_b32 v2, v2, 15, v47
	v_lshl_or_b32 v2, v46, 11, v2
	v_lshl_add_u64 v[140:141], s[18:19], 0, v[2:3]
	v_lshl_add_u64 v[142:143], s[2:3], 0, v[2:3]
	s_mov_b32 s21, 0
	s_mov_b64 s[0:1], 0
	s_mov_b64 s[2:3], 0x100
	s_mov_b64 s[8:9], 0x20100
	s_mov_b64 s[16:17], 0x40100
	s_mov_b64 s[18:19], 0x60100
	v_mov_b32_e32 v2, v3
	v_mov_b32_e32 v4, v3
	v_mov_b32_e32 v5, v3
	v_mov_b32_e32 v46, v3
	v_mov_b32_e32 v47, v3
.LBB2_1:
	s_mul_i32 s22, s21, 0xe000
	v_add_u32_e32 v196, s22, v214
	v_add_u32_e32 v197, s22, v215
	s_add_u32 s46, s22, s45
	s_add_i32 s21, s21, 1
	s_waitcnt lgkmcnt(0)
	v_mfma_f32_16x16x32_f16 v[130:133], v[22:25], v[42:45], v[130:133]
	ds_read_b128 v[154:157], v196
	ds_read_b128 v[158:161], v196 offset:2048
	v_mfma_f32_16x16x32_f16 v[98:101], v[18:21], v[42:45], v[98:101]
	ds_read_b128 v[162:165], v196 offset:4096
	ds_read_b128 v[166:169], v196 offset:6144
	v_mfma_f32_16x16x32_f16 v[86:89], v[30:33], v[42:45], v[86:89]
	ds_read_b128 v[170:173], v197 offset:32768
	ds_read_b128 v[174:177], v197 offset:34816
	v_mfma_f32_16x16x32_f16 v[74:77], v[26:29], v[42:45], v[74:77]
	ds_read_b128 v[178:181], v197 offset:36864
	ds_read_b128 v[182:185], v197 offset:38912
	v_mfma_f32_16x16x32_f16 v[70:73], v[42:45], v[34:37], v[70:73]
	ds_read_b128 v[186:189], v197 offset:40960
	ds_read_b128 v[190:193], v197 offset:43008
	v_mfma_f32_16x16x32_f16 v[66:69], v[42:45], v[14:17], v[66:69]
	v_mfma_f32_16x16x32_f16 v[62:65], v[22:25], v[38:41], v[62:65]
	v_mfma_f32_16x16x32_f16 v[58:61], v[18:21], v[38:41], v[58:61]
	v_mfma_f32_16x16x32_f16 v[54:57], v[30:33], v[38:41], v[54:57]
	v_mfma_f32_16x16x32_f16 v[50:53], v[26:29], v[38:41], v[50:53]
	v_mfma_f32_16x16x32_f16 v[46:49], v[38:41], v[34:37], v[46:49]
	v_mfma_f32_16x16x32_f16 v[2:5], v[38:41], v[14:17], v[2:5]
	v_mfma_f32_16x16x32_f16 v[78:81], v[22:25], v[10:13], v[78:81]
	v_mfma_f32_16x16x32_f16 v[82:85], v[18:21], v[10:13], v[82:85]
	v_mfma_f32_16x16x32_f16 v[90:93], v[30:33], v[10:13], v[90:93]
	v_mfma_f32_16x16x32_f16 v[94:97], v[26:29], v[10:13], v[94:97]
	v_mfma_f32_16x16x32_f16 v[102:105], v[10:13], v[34:37], v[102:105]
	v_mfma_f32_16x16x32_f16 v[106:109], v[10:13], v[14:17], v[106:109]
	v_mfma_f32_16x16x32_f16 v[110:113], v[22:25], v[6:9], v[110:113]
	v_mfma_f32_16x16x32_f16 v[114:117], v[18:21], v[6:9], v[114:117]
	v_mfma_f32_16x16x32_f16 v[118:121], v[30:33], v[6:9], v[118:121]
	v_mfma_f32_16x16x32_f16 v[122:125], v[26:29], v[6:9], v[122:125]
	v_mfma_f32_16x16x32_f16 v[134:137], v[6:9], v[34:37], v[134:137]
	v_mfma_f32_16x16x32_f16 v[126:129], v[6:9], v[14:17], v[126:129]
	s_cmp_lg_u32 s21, 2
	s_cselect_b32 s21, s21, 0
	s_mul_i32 s22, s21, 0xe000
	v_add_u32_e32 v196, s22, v146
	v_add_u32_e32 v197, s22, v153
	s_waitcnt vmcnt(0) lgkmcnt(0)
	s_barrier
	s_mov_b32 m0, s46
	s_nop 0
	global_load_lds_dwordx4 v194, s[24:25]
	s_add_u32 m0, s46, 0x2000
	s_nop 0
	global_load_lds_dwordx4 v194, s[26:27]
	s_add_u32 m0, s46, 0x4000
	s_nop 0
	global_load_lds_dwordx4 v194, s[28:29]
	s_add_u32 m0, s46, 0x6000
	s_nop 0
	global_load_lds_dwordx4 v194, s[30:31]
	s_add_u32 m0, s46, 0x8000
	s_nop 0
	global_load_lds_dwordx4 v194, s[32:33]
	s_add_u32 m0, s46, 0xa000
	s_nop 0
	global_load_lds_dwordx4 v194, s[34:35]
	s_add_u32 m0, s46, 0xc000
	s_nop 0
	global_load_lds_dwordx4 v194, s[36:37]
	v_add_u32_e32 v194, 0x80, v194
	v_mfma_f32_16x16x32_f16 v[130:133], v[170:173], v[154:157], v[130:133]
	ds_read_b128 v[42:45], v196
	ds_read_b128 v[38:41], v196 offset:2048
	v_mfma_f32_16x16x32_f16 v[98:101], v[174:177], v[154:157], v[98:101]
	ds_read_b128 v[10:13], v196 offset:4096
	ds_read_b128 v[6:9], v196 offset:6144
	v_mfma_f32_16x16x32_f16 v[86:89], v[178:181], v[154:157], v[86:89]
	ds_read_b128 v[22:25], v197 offset:32768
	ds_read_b128 v[18:21], v197 offset:34816
	v_mfma_f32_16x16x32_f16 v[74:77], v[182:185], v[154:157], v[74:77]
	ds_read_b128 v[30:33], v197 offset:36864
	ds_read_b128 v[26:29], v197 offset:38912
	v_mfma_f32_16x16x32_f16 v[70:73], v[154:157], v[186:189], v[70:73]
	ds_read_b128 v[34:37], v197 offset:40960
	ds_read_b128 v[14:17], v197 offset:43008
	v_mfma_f32_16x16x32_f16 v[66:69], v[154:157], v[190:193], v[66:69]
	v_mfma_f32_16x16x32_f16 v[62:65], v[170:173], v[158:161], v[62:65]
	v_mfma_f32_16x16x32_f16 v[58:61], v[174:177], v[158:161], v[58:61]
	v_mfma_f32_16x16x32_f16 v[54:57], v[178:181], v[158:161], v[54:57]
	v_mfma_f32_16x16x32_f16 v[50:53], v[182:185], v[158:161], v[50:53]
	v_mfma_f32_16x16x32_f16 v[46:49], v[158:161], v[186:189], v[46:49]
	v_mfma_f32_16x16x32_f16 v[2:5], v[158:161], v[190:193], v[2:5]
	v_mfma_f32_16x16x32_f16 v[78:81], v[170:173], v[162:165], v[78:81]
	v_mfma_f32_16x16x32_f16 v[82:85], v[174:177], v[162:165], v[82:85]
	v_mfma_f32_16x16x32_f16 v[90:93], v[178:181], v[162:165], v[90:93]
	v_mfma_f32_16x16x32_f16 v[94:97], v[182:185], v[162:165], v[94:97]
	v_mfma_f32_16x16x32_f16 v[102:105], v[162:165], v[186:189], v[102:105]
	v_mfma_f32_16x16x32_f16 v[106:109], v[162:165], v[190:193], v[106:109]
	v_mfma_f32_16x16x32_f16 v[110:113], v[170:173], v[166:169], v[110:113]
	v_mfma_f32_16x16x32_f16 v[114:117], v[174:177], v[166:169], v[114:117]
	v_mfma_f32_16x16x32_f16 v[118:121], v[178:181], v[166:169], v[118:121]
	v_mfma_f32_16x16x32_f16 v[122:125], v[182:185], v[166:169], v[122:125]
	v_mfma_f32_16x16x32_f16 v[134:137], v[166:169], v[186:189], v[134:137]
	v_mfma_f32_16x16x32_f16 v[126:129], v[166:169], v[190:193], v[126:129]
	s_add_u32 s0, s0, 0x80
	s_addc_u32 s1, s1, 0
	s_cmpk_eq_i32 s0, 0x700
	s_cbranch_scc0 .LBB2_1
	s_waitcnt lgkmcnt(0)
	v_mfma_f32_16x16x32_f16 v[130:133], v[22:25], v[42:45], v[130:133]
	ds_read_b128 v[140:143], v214
	ds_read_b128 v[154:157], v214 offset:2048
	v_mfma_f32_16x16x32_f16 v[98:101], v[18:21], v[42:45], v[98:101]
	ds_read_b128 v[158:161], v214 offset:4096
	ds_read_b128 v[162:165], v214 offset:6144
	v_mfma_f32_16x16x32_f16 v[86:89], v[30:33], v[42:45], v[86:89]
	ds_read_b128 v[166:169], v215 offset:32768
	ds_read_b128 v[170:173], v215 offset:34816
	v_mfma_f32_16x16x32_f16 v[74:77], v[26:29], v[42:45], v[74:77]
	ds_read_b128 v[174:177], v215 offset:36864
	ds_read_b128 v[178:181], v215 offset:38912
	v_mfma_f32_16x16x32_f16 v[70:73], v[42:45], v[34:37], v[70:73]
	ds_read_b128 v[182:185], v215 offset:40960
	ds_read_b128 v[186:189], v215 offset:43008
	v_mfma_f32_16x16x32_f16 v[42:45], v[42:45], v[14:17], v[66:69]
	v_mfma_f32_16x16x32_f16 v[62:65], v[22:25], v[38:41], v[62:65]
	v_mfma_f32_16x16x32_f16 v[58:61], v[18:21], v[38:41], v[58:61]
	v_mfma_f32_16x16x32_f16 v[54:57], v[30:33], v[38:41], v[54:57]
	v_mfma_f32_16x16x32_f16 v[50:53], v[26:29], v[38:41], v[50:53]
	v_mfma_f32_16x16x32_f16 v[46:49], v[38:41], v[34:37], v[46:49]
	v_mfma_f32_16x16x32_f16 v[2:5], v[38:41], v[14:17], v[2:5]
	v_mfma_f32_16x16x32_f16 v[38:41], v[22:25], v[10:13], v[78:81]
	v_mfma_f32_16x16x32_f16 v[66:69], v[18:21], v[10:13], v[82:85]
	v_mfma_f32_16x16x32_f16 v[78:81], v[30:33], v[10:13], v[90:93]
	v_mfma_f32_16x16x32_f16 v[82:85], v[26:29], v[10:13], v[94:97]
	v_mfma_f32_16x16x32_f16 v[90:93], v[10:13], v[34:37], v[102:105]
	v_mfma_f32_16x16x32_f16 v[94:97], v[10:13], v[14:17], v[106:109]
	v_mfma_f32_16x16x32_f16 v[22:25], v[22:25], v[6:9], v[110:113]
	v_mfma_f32_16x16x32_f16 v[102:105], v[18:21], v[6:9], v[114:117]
	v_or_b32_e32 v21, v151, v152
	v_and_b32_e32 v20, 63, v0
	v_mfma_f32_16x16x32_f16 v[30:33], v[30:33], v[6:9], v[118:121]
	v_mfma_f32_16x16x32_f16 v[26:29], v[26:29], v[6:9], v[122:125]
	v_mfma_f32_16x16x32_f16 v[34:37], v[6:9], v[34:37], v[134:137]
	v_mfma_f32_16x16x32_f16 v[6:9], v[6:9], v[14:17], v[126:129]
	v_add_u32_e32 v10, 0x16800, v21
	s_waitcnt vmcnt(0) lgkmcnt(0)
	s_waitcnt lgkmcnt(0)
	v_mfma_f32_16x16x32_f16 v[16:19], v[166:169], v[140:143], v[130:133]
	s_barrier
	ds_read_b128 v[106:109], v146 offset:57344
	ds_read_b128 v[110:113], v146 offset:59392
	v_mfma_f32_16x16x32_f16 v[98:101], v[170:173], v[140:143], v[98:101]
	ds_read_b128 v[114:117], v146 offset:61440
	ds_read_b128 v[12:15], v146 offset:63488
	v_add_u32_e32 v0, 0x16000, v21
	v_mfma_f32_16x16x32_f16 v[86:89], v[174:177], v[140:143], v[86:89]
	ds_read_b128 v[122:125], v10
	v_add_u32_e32 v10, 0x17000, v21
	ds_read_b128 v[118:121], v0
	v_mfma_f32_16x16x32_f16 v[74:77], v[178:181], v[140:143], v[74:77]
	ds_read_b128 v[126:129], v10
	v_add_u32_e32 v10, 0x17800, v21
	ds_read_b128 v[130:133], v10
	v_mfma_f32_16x16x32_f16 v[70:73], v[140:143], v[182:185], v[70:73]
	ds_read_b128 v[134:137], v0 offset:8192
	ds_read_b128 v[190:193], v0 offset:10240
	v_mfma_f32_16x16x32_f16 v[42:45], v[140:143], v[186:189], v[42:45]
	v_mfma_f32_16x16x32_f16 v[62:65], v[166:169], v[154:157], v[62:65]
	v_mfma_f32_16x16x32_f16 v[58:61], v[170:173], v[154:157], v[58:61]
	v_mfma_f32_16x16x32_f16 v[54:57], v[174:177], v[154:157], v[54:57]
	v_mfma_f32_16x16x32_f16 v[50:53], v[178:181], v[154:157], v[50:53]
	v_mfma_f32_16x16x32_f16 v[46:49], v[154:157], v[182:185], v[46:49]
	v_mfma_f32_16x16x32_f16 v[140:143], v[154:157], v[186:189], v[2:5]
	v_mfma_f32_16x16x32_f16 v[38:41], v[166:169], v[158:161], v[38:41]
	v_mfma_f32_16x16x32_f16 v[66:69], v[170:173], v[158:161], v[66:69]
	v_mfma_f32_16x16x32_f16 v[78:81], v[174:177], v[158:161], v[78:81]
	v_mfma_f32_16x16x32_f16 v[82:85], v[178:181], v[158:161], v[82:85]
	v_mfma_f32_16x16x32_f16 v[90:93], v[158:161], v[182:185], v[90:93]
	v_mfma_f32_16x16x32_f16 v[94:97], v[158:161], v[186:189], v[94:97]
	v_mfma_f32_16x16x32_f16 v[22:25], v[166:169], v[162:165], v[22:25]
	v_mfma_f32_16x16x32_f16 v[102:105], v[170:173], v[162:165], v[102:105]
	v_mfma_f32_16x16x32_f16 v[30:33], v[174:177], v[162:165], v[30:33]
	v_mfma_f32_16x16x32_f16 v[26:29], v[178:181], v[162:165], v[26:29]
	v_mfma_f32_16x16x32_f16 v[34:37], v[162:165], v[182:185], v[34:37]
	v_mfma_f32_16x16x32_f16 v[152:155], v[162:165], v[186:189], v[6:9]
	s_waitcnt lgkmcnt(0)
	v_mfma_f32_16x16x32_f16 v[156:159], v[118:121], v[106:109], v[16:19]
	s_movk_i32 s0, 0x7c0
	v_add_u32_e32 v216, 0x16000, v215
	ds_read_b128 v[202:205], v216 offset:8192
	ds_read_b128 v[206:209], v216 offset:10240
	v_lshlrev_b32_e32 v16, 6, v144
	v_mov_b32_e32 v17, 0
	v_mov_b32_e32 v139, v17
	v_lshl_add_u64 v[4:5], s[6:7], 0, v[16:17]
	v_lshl_add_u64 v[8:9], v[4:5], 0, v[138:139]
	s_waitcnt vmcnt(0)
	v_lshlrev_b32_e32 v4, 5, v150
	v_lshl_add_u64 v[2:3], s[4:5], 0, v[16:17]
	v_ashrrev_i32_e32 v5, 31, v4
	v_lshl_add_u64 v[2:3], v[2:3], 0, v[138:139]
	v_lshlrev_b64 v[4:5], 2, v[4:5]
	v_lshl_add_u64 v[6:7], v[2:3], 0, v[4:5]
	v_lshl_add_u64 v[4:5], v[8:9], 0, v[4:5]
	v_mfma_f32_16x16x32_f16 v[98:101], v[122:125], v[106:109], v[98:101]
	global_load_dwordx4 v[160:163], v[6:7], off
	v_lshlrev_b32_e32 v18, 5, v147
	v_ashrrev_i32_e32 v19, 31, v18
	v_mfma_f32_16x16x32_f16 v[86:89], v[126:129], v[106:109], v[86:89]
	v_lshlrev_b64 v[18:19], 2, v[18:19]
	ds_read_b128 v[172:175], v214 offset:61440
	ds_read_b128 v[176:179], v214 offset:63488
	v_mfma_f32_16x16x32_f16 v[74:77], v[130:133], v[106:109], v[74:77]
	v_mfma_f32_16x16x32_f16 v[70:73], v[106:109], v[134:137], v[70:73]
	v_mfma_f32_16x16x32_f16 v[42:45], v[106:109], v[190:193], v[42:45]
	global_load_dwordx4 v[106:109], v[4:5], off
	v_lshlrev_b32_e32 v4, 5, v149
	v_ashrrev_i32_e32 v5, 31, v4
	v_lshlrev_b64 v[4:5], 2, v[4:5]
	v_lshl_add_u64 v[6:7], v[2:3], 0, v[4:5]
	v_lshl_add_u64 v[4:5], v[8:9], 0, v[4:5]
	global_load_dwordx4 v[168:171], v[4:5], off
	global_load_dwordx4 v[164:167], v[6:7], off
	v_lshlrev_b32_e32 v4, 5, v148
	v_ashrrev_i32_e32 v5, 31, v4
	v_lshlrev_b64 v[10:11], 2, v[4:5]
	v_lshl_add_u64 v[4:5], v[2:3], 0, v[10:11]
	v_lshl_add_u64 v[10:11], v[8:9], 0, v[10:11]
	global_load_dwordx4 v[210:213], v[10:11], off
	v_lshl_add_u64 v[2:3], v[2:3], 0, v[18:19]
	global_load_dwordx4 v[4:7], v[4:5], off
	v_lshl_add_u64 v[8:9], v[8:9], 0, v[18:19]
	v_add_u32_e32 v18, 0x16000, v215
	v_ashrrev_i32_e32 v10, 7, v145
	ds_read_b128 v[180:183], v18
	v_add_u32_e32 v18, 0x17000, v215
	v_and_b32_e32 v10, -16, v10
	v_add_u32_e32 v19, 0x16800, v215
	ds_read_b128 v[194:197], v18
	v_add_u32_e32 v18, s20, v10
	global_load_dwordx4 v[8:11], v[8:9], off
	ds_read_b128 v[184:187], v19
	v_add_u32_e32 v19, 0x17800, v215
	v_and_or_b32 v21, v145, s0, v1
	global_load_dwordx4 v[0:3], v[2:3], off
	v_mfma_f32_16x16x32_f16 v[62:65], v[118:121], v[110:113], v[62:65]
	ds_read_b128 v[198:201], v19
	v_ashrrev_i32_e32 v19, 31, v18
	ds_read_b128 v[148:151], v214 offset:59392
	v_mfma_f32_16x16x32_f16 v[58:61], v[122:125], v[110:113], v[58:61]
	v_mfma_f32_16x16x32_f16 v[54:57], v[126:129], v[110:113], v[54:57]
	v_mfma_f32_16x16x32_f16 v[50:53], v[130:133], v[110:113], v[50:53]
	v_mfma_f32_16x16x32_f16 v[46:49], v[110:113], v[134:137], v[46:49]
	v_mfma_f32_16x16x32_f16 v[110:113], v[110:113], v[190:193], v[140:143]
	s_nop 2
	ds_read_b128 v[140:143], v214 offset:57344
	v_mfma_f32_16x16x32_f16 v[38:41], v[118:121], v[114:117], v[38:41]
	v_mfma_f32_16x16x32_f16 v[66:69], v[122:125], v[114:117], v[66:69]
	v_mfma_f32_16x16x32_f16 v[78:81], v[126:129], v[114:117], v[78:81]
	v_mfma_f32_16x16x32_f16 v[82:85], v[130:133], v[114:117], v[82:85]
	v_mfma_f32_16x16x32_f16 v[90:93], v[114:117], v[134:137], v[90:93]
	v_mfma_f32_16x16x32_f16 v[94:97], v[114:117], v[190:193], v[94:97]
	s_waitcnt lgkmcnt(0)
	v_mfma_f32_16x16x32_f16 v[114:117], v[180:183], v[140:143], v[156:159]
	v_mfma_f32_16x16x32_f16 v[98:101], v[184:187], v[140:143], v[98:101]
	v_mfma_f32_16x16x32_f16 v[22:25], v[118:121], v[12:15], v[22:25]
	s_waitcnt vmcnt(6)
	s_nop 4
	v_pk_mul_f32 v[120:121], v[114:115], v[106:107] op_sel_hi:[1,0]
	v_lshlrev_b64 v[118:119], 17, v[18:19]
	v_lshl_or_b32 v118, v21, 6, v118
	v_mfma_f32_16x16x32_f16 v[102:105], v[122:125], v[12:15], v[102:105]
	v_mul_f32_e64 v122, v116, v107
	v_mul_f32_e64 v123, v117, v107
	v_pk_fma_f32 v[124:125], v[114:115], v[160:161], v[120:121] op_sel:[0,0,1] op_sel_hi:[1,1,0] neg_lo:[0,0,1] neg_hi:[0,0,1]
	v_pk_fma_f32 v[114:115], v[114:115], v[160:161], v[120:121] op_sel:[0,0,1] op_sel_hi:[1,0,0]
	v_pk_fma_f32 v[120:121], v[116:117], v[160:161], v[122:123] op_sel:[0,1,1] op_sel_hi:[1,1,0] neg_lo:[0,0,1] neg_hi:[0,0,1]
	v_pk_fma_f32 v[116:117], v[116:117], v[160:161], v[122:123] op_sel:[0,1,1] op_sel_hi:[1,1,0]
	v_cvt_pk_f16_f32 v114, v124, v115
	v_cvt_pk_f16_f32 v115, v120, v117
	v_pk_mul_f32 v[116:117], v[98:99], v[108:109] op_sel_hi:[1,0]
	v_mov_b32_e32 v122, v163
	v_pk_fma_f32 v[120:121], v[98:99], v[162:163], v[116:117] op_sel:[0,0,1] op_sel_hi:[1,1,0] neg_lo:[0,0,1] neg_hi:[0,0,1]
	v_pk_fma_f32 v[98:99], v[98:99], v[162:163], v[116:117] op_sel:[0,0,1] op_sel_hi:[1,0,0]
	v_mfma_f32_16x16x32_f16 v[30:33], v[126:129], v[12:15], v[30:33]
	v_cvt_pk_f16_f32 v116, v120, v99
	v_mov_b32_e32 v120, v109
	v_pk_mul_f32 v[98:99], v[100:101], v[120:121] op_sel_hi:[1,0]
	v_mfma_f32_16x16x32_f16 v[26:29], v[130:133], v[12:15], v[26:29]
	v_fma_f32 v124, v100, v122, -v99
	v_fma_f32 v125, v101, v122, -v98
	v_pk_fma_f32 v[98:99], v[100:101], v[122:123], v[98:99] op_sel:[0,0,1] op_sel_hi:[1,0,0]
	s_nop 0
	v_cvt_pk_f16_f32 v117, v124, v99
	v_lshlrev_b64 v[124:125], 1, v[118:119]
	v_lshl_add_u64 v[126:127], s[10:11], 0, v[124:125]
	v_mfma_f32_16x16x32_f16 v[34:37], v[12:15], v[134:137], v[34:37]
	v_mfma_f32_16x16x32_f16 v[98:101], v[12:15], v[190:193], v[152:155]
	v_lshl_add_u64 v[12:13], v[126:127], 0, v[16:17]
	v_lshl_add_u64 v[126:127], v[12:13], 0, v[138:139]
	global_store_dwordx4 v[126:127], v[114:117], off sc1
	v_mfma_f32_16x16x32_f16 v[12:15], v[194:197], v[140:143], v[86:89]
	v_mfma_f32_16x16x32_f16 v[74:77], v[198:201], v[140:143], v[74:77]
	v_mfma_f32_16x16x32_f16 v[58:61], v[184:187], v[148:151], v[58:61]
	s_nop 5
	v_mul_f32_e64 v86, v12, v106
	v_mul_f32_e64 v87, v13, v106
	v_pk_fma_f32 v[88:89], v[12:13], v[160:161], v[86:87] op_sel:[0,0,1] op_sel_hi:[1,1,0] neg_lo:[0,0,1] neg_hi:[0,0,1]
	v_pk_fma_f32 v[12:13], v[12:13], v[160:161], v[86:87] op_sel:[0,0,1] op_sel_hi:[1,0,0]
	v_mfma_f32_16x16x32_f16 v[54:57], v[194:197], v[148:151], v[54:57]
	v_cvt_pk_f16_f32 v86, v88, v13
	v_pk_mul_f32 v[12:13], v[14:15], v[106:107] op_sel:[0,1]
	s_nop 0
	v_pk_fma_f32 v[88:89], v[14:15], v[160:161], v[12:13] op_sel:[0,1,1] op_sel_hi:[1,1,0] neg_lo:[0,0,1] neg_hi:[0,0,1]
	v_pk_fma_f32 v[12:13], v[14:15], v[160:161], v[12:13] op_sel:[0,1,1] op_sel_hi:[1,1,0]
	v_mfma_f32_16x16x32_f16 v[50:53], v[198:201], v[148:151], v[50:53]
	v_cvt_pk_f16_f32 v87, v88, v13
	v_pk_mul_f32 v[88:89], v[74:75], v[108:109] op_sel_hi:[1,0]
	v_mfma_f32_16x16x32_f16 v[12:15], v[140:143], v[206:209], v[42:45]
	s_nop 2
	v_fma_f32 v42, v74, v162, -v89
	v_fma_f32 v43, v75, v163, -v88
	v_pk_fma_f32 v[44:45], v[74:75], v[162:163], v[88:89] op_sel:[0,0,1] op_sel_hi:[1,0,0]
	v_mfma_f32_16x16x32_f16 v[38:41], v[180:183], v[172:175], v[38:41]
	v_cvt_pk_f16_f32 v88, v42, v45
	v_mfma_f32_16x16x32_f16 v[42:45], v[180:183], v[148:151], v[62:65]
	s_nop 2
	v_mul_f32_e64 v62, v76, v120
	v_mul_f32_e64 v63, v77, v120
	v_mfma_f32_16x16x32_f16 v[66:69], v[184:187], v[172:175], v[66:69]
	v_fma_f32 v64, v76, v122, -v63
	v_fma_f32 v65, v77, v122, -v62
	v_pk_fma_f32 v[62:63], v[76:77], v[122:123], v[62:63] op_sel:[0,0,1] op_sel_hi:[1,0,0]
	s_nop 0
	v_cvt_pk_f16_f32 v89, v64, v63
	v_lshl_add_u64 v[62:63], s[12:13], 0, v[124:125]
	v_lshl_add_u64 v[62:63], v[62:63], 0, v[16:17]
	v_lshl_add_u64 v[106:107], v[62:63], 0, v[138:139]
	s_waitcnt vmcnt(6)
	v_pk_mul_f32 v[62:63], v[42:43], v[168:169] op_sel_hi:[1,0]
	global_store_dwordx4 v[106:107], v[86:89], off sc1
	s_waitcnt vmcnt(6)
	v_pk_fma_f32 v[64:65], v[42:43], v[164:165], v[62:63] op_sel:[0,0,1] op_sel_hi:[1,1,0] neg_lo:[0,0,1] neg_hi:[0,0,1]
	v_pk_fma_f32 v[42:43], v[42:43], v[164:165], v[62:63] op_sel:[0,0,1] op_sel_hi:[1,0,0]
	v_pk_mul_f32 v[62:63], v[44:45], v[168:169] op_sel:[0,1]
	v_cvt_pk_f16_f32 v42, v64, v43
	v_pk_fma_f32 v[74:75], v[44:45], v[164:165], v[62:63] op_sel:[0,1,1] op_sel_hi:[1,1,0] neg_lo:[0,0,1] neg_hi:[0,0,1]
	v_pk_fma_f32 v[44:45], v[44:45], v[164:165], v[62:63] op_sel:[0,1,1] op_sel_hi:[1,1,0]
	v_mov_b32_e32 v86, v171
	v_cvt_pk_f16_f32 v43, v74, v45
	v_pk_mul_f32 v[44:45], v[58:59], v[170:171] op_sel_hi:[1,0]
	v_mov_b32_e32 v88, v167
	v_pk_fma_f32 v[74:75], v[58:59], v[166:167], v[44:45] op_sel:[0,0,1] op_sel_hi:[1,1,0] neg_lo:[0,0,1] neg_hi:[0,0,1]
	v_pk_fma_f32 v[44:45], v[58:59], v[166:167], v[44:45] op_sel:[0,0,1] op_sel_hi:[1,0,0]
	v_pk_mul_f32 v[58:59], v[60:61], v[86:87] op_sel_hi:[1,0]
	v_cvt_pk_f16_f32 v44, v74, v45
	v_pk_fma_f32 v[108:109], v[60:61], v[88:89], v[58:59] op_sel:[0,0,1] op_sel_hi:[1,0,0] neg_lo:[0,0,1] neg_hi:[0,0,1]
	v_pk_fma_f32 v[58:59], v[60:61], v[88:89], v[58:59] op_sel:[0,0,1] op_sel_hi:[1,0,0]
	v_mfma_f32_16x16x32_f16 v[74:77], v[194:197], v[172:175], v[78:81]
	v_cvt_pk_f16_f32 v45, v108, v59
	global_store_dwordx4 v[126:127], v[42:45], off offset:2048 sc1
	v_pk_mul_f32 v[58:59], v[54:55], v[168:169] op_sel_hi:[1,0]
	v_mfma_f32_16x16x32_f16 v[22:25], v[180:183], v[176:179], v[22:25]
	v_fma_f32 v78, v54, v164, -v59
	v_fma_f32 v79, v55, v165, -v58
	v_pk_fma_f32 v[54:55], v[54:55], v[164:165], v[58:59] op_sel:[0,0,1] op_sel_hi:[1,0,0]
	v_mfma_f32_16x16x32_f16 v[42:45], v[198:201], v[172:175], v[82:85]
	v_cvt_pk_f16_f32 v54, v78, v55
	s_nop 1
	v_pk_mul_f32 v[82:83], v[56:57], v[168:169] op_sel:[0,1]
	v_mfma_f32_16x16x32_f16 v[30:33], v[194:197], v[176:179], v[30:33]
	v_fma_f32 v84, v56, v165, -v83
	v_fma_f32 v85, v57, v165, -v82
	v_pk_fma_f32 v[56:57], v[56:57], v[164:165], v[82:83] op_sel:[0,1,1] op_sel_hi:[1,1,0]
	s_nop 0
	v_cvt_pk_f16_f32 v55, v84, v57
	v_pk_mul_f32 v[56:57], v[50:51], v[170:171] op_sel_hi:[1,0]
	v_mfma_f32_16x16x32_f16 v[26:29], v[198:201], v[176:179], v[26:29]
	v_fma_f32 v82, v50, v166, -v57
	v_fma_f32 v83, v51, v167, -v56
	v_pk_fma_f32 v[50:51], v[50:51], v[166:167], v[56:57] op_sel:[0,0,1] op_sel_hi:[1,0,0]
	s_nop 0
	v_cvt_pk_f16_f32 v56, v82, v51
	v_pk_mul_f32 v[50:51], v[52:53], v[86:87] op_sel_hi:[1,0]
	v_mfma_f32_16x16x32_f16 v[82:85], v[184:187], v[176:179], v[102:105]
	v_fma_f32 v86, v52, v88, -v51
	v_fma_f32 v87, v53, v88, -v50
	v_pk_fma_f32 v[50:51], v[52:53], v[88:89], v[50:51] op_sel:[0,0,1] op_sel_hi:[1,0,0]
	s_nop 0
	v_cvt_pk_f16_f32 v57, v86, v51
	global_store_dwordx4 v[106:107], v[54:57], off offset:2048 sc1
	s_waitcnt vmcnt(7)
	v_pk_mul_f32 v[50:51], v[38:39], v[210:211] op_sel_hi:[1,0]
	v_mfma_f32_16x16x32_f16 v[70:73], v[140:143], v[202:205], v[70:73]
	v_mul_f32_e64 v56, v40, v211
	v_mul_f32_e64 v57, v41, v211
	s_waitcnt vmcnt(6)
	v_pk_fma_f32 v[52:53], v[38:39], v[4:5], v[50:51] op_sel:[0,0,1] op_sel_hi:[1,1,0] neg_lo:[0,0,1] neg_hi:[0,0,1]
	v_pk_fma_f32 v[38:39], v[38:39], v[4:5], v[50:51] op_sel:[0,0,1] op_sel_hi:[1,0,0]
	v_pk_fma_f32 v[86:87], v[40:41], v[4:5], v[56:57] op_sel:[0,1,1] op_sel_hi:[1,1,0] neg_lo:[0,0,1] neg_hi:[0,0,1]
	v_pk_fma_f32 v[40:41], v[40:41], v[4:5], v[56:57] op_sel:[0,1,1] op_sel_hi:[1,1,0]
	v_cvt_pk_f16_f32 v38, v52, v39
	v_cvt_pk_f16_f32 v39, v86, v41
	v_pk_mul_f32 v[40:41], v[66:67], v[212:213] op_sel_hi:[1,0]
	v_or_b32_e32 v54, 0x800, v118
	v_pk_fma_f32 v[56:57], v[66:67], v[6:7], v[40:41] op_sel:[0,0,1] op_sel_hi:[1,1,0] neg_lo:[0,0,1] neg_hi:[0,0,1]
	v_pk_fma_f32 v[40:41], v[66:67], v[6:7], v[40:41] op_sel:[0,0,1] op_sel_hi:[1,0,0]
	v_mov_b32_e32 v55, v119
	v_cvt_pk_f16_f32 v40, v56, v41
	v_mov_b32_e32 v56, v213
	v_pk_mul_f32 v[66:67], v[68:69], v[56:57] op_sel_hi:[1,0]
	v_mov_b32_e32 v86, v7
	v_pk_fma_f32 v[88:89], v[68:69], v[86:87], v[66:67] op_sel:[0,0,1] op_sel_hi:[1,0,0] neg_lo:[0,0,1] neg_hi:[0,0,1]
	v_pk_fma_f32 v[66:67], v[68:69], v[86:87], v[66:67] op_sel:[0,0,1] op_sel_hi:[1,0,0]
	v_lshlrev_b64 v[54:55], 1, v[54:55]
	v_cvt_pk_f16_f32 v41, v88, v67
	v_lshl_add_u64 v[66:67], s[10:11], 0, v[54:55]
	v_lshl_add_u64 v[66:67], v[66:67], 0, v[16:17]
	v_lshl_add_u64 v[66:67], v[66:67], 0, v[138:139]
	global_store_dwordx4 v[66:67], v[38:41], off sc1
	v_or_b32_e32 v118, 0xc00, v118
	v_mfma_f32_16x16x32_f16 v[46:49], v[148:151], v[202:205], v[46:49]
	v_mul_f32_e64 v38, v74, v210
	v_mul_f32_e64 v39, v75, v210
	v_pk_fma_f32 v[40:41], v[74:75], v[4:5], v[38:39] op_sel:[0,0,1] op_sel_hi:[1,1,0] neg_lo:[0,0,1] neg_hi:[0,0,1]
	v_pk_fma_f32 v[38:39], v[74:75], v[4:5], v[38:39] op_sel:[0,0,1] op_sel_hi:[1,0,0]
	v_mfma_f32_16x16x32_f16 v[58:61], v[172:175], v[202:205], v[90:93]
	v_cvt_pk_f16_f32 v38, v40, v39
	v_pk_mul_f32 v[40:41], v[76:77], v[210:211] op_sel:[0,1]
	s_nop 0
	v_pk_fma_f32 v[66:67], v[76:77], v[4:5], v[40:41] op_sel:[0,1,1] op_sel_hi:[1,1,0] neg_lo:[0,0,1] neg_hi:[0,0,1]
	v_pk_fma_f32 v[4:5], v[76:77], v[4:5], v[40:41] op_sel:[0,1,1] op_sel_hi:[1,1,0]
	v_mfma_f32_16x16x32_f16 v[34:37], v[176:179], v[202:205], v[34:37]
	v_cvt_pk_f16_f32 v39, v66, v5
	v_pk_mul_f32 v[4:5], v[42:43], v[212:213] op_sel_hi:[1,0]
	s_nop 0
	v_pk_fma_f32 v[40:41], v[42:43], v[6:7], v[4:5] op_sel:[0,0,1] op_sel_hi:[1,1,0] neg_lo:[0,0,1] neg_hi:[0,0,1]
	v_pk_fma_f32 v[4:5], v[42:43], v[6:7], v[4:5] op_sel:[0,0,1] op_sel_hi:[1,0,0]
	v_mfma_f32_16x16x32_f16 v[62:65], v[148:151], v[206:209], v[110:113]
	v_cvt_pk_f16_f32 v40, v40, v5
	v_pk_mul_f32 v[4:5], v[44:45], v[56:57] op_sel_hi:[1,0]
	s_nop 0
	v_pk_fma_f32 v[6:7], v[44:45], v[86:87], v[4:5] op_sel:[0,0,1] op_sel_hi:[1,0,0] neg_lo:[0,0,1] neg_hi:[0,0,1]
	v_pk_fma_f32 v[4:5], v[44:45], v[86:87], v[4:5] op_sel:[0,0,1] op_sel_hi:[1,0,0]
	v_mfma_f32_16x16x32_f16 v[78:81], v[172:175], v[206:209], v[94:97]
	v_cvt_pk_f16_f32 v41, v6, v5
	v_lshl_add_u64 v[4:5], s[12:13], 0, v[54:55]
	v_lshl_add_u64 v[4:5], v[4:5], 0, v[16:17]
	v_lshl_add_u64 v[4:5], v[4:5], 0, v[138:139]
	global_store_dwordx4 v[4:5], v[38:41], off sc1
	s_waitcnt vmcnt(7)
	v_pk_mul_f32 v[4:5], v[22:23], v[8:9] op_sel_hi:[1,0]
	v_mfma_f32_16x16x32_f16 v[50:53], v[176:179], v[206:209], v[98:101]
	s_waitcnt vmcnt(6)
	v_pk_fma_f32 v[6:7], v[22:23], v[0:1], v[4:5] op_sel:[0,0,1] op_sel_hi:[1,1,0] neg_lo:[0,0,1] neg_hi:[0,0,1]
	v_pk_fma_f32 v[4:5], v[22:23], v[0:1], v[4:5] op_sel:[0,0,1] op_sel_hi:[1,0,0]
	v_mov_b32_e32 v38, v3
	v_cvt_pk_f16_f32 v4, v6, v5
	v_pk_mul_f32 v[6:7], v[24:25], v[8:9] op_sel:[0,1]
	s_nop 0
	v_pk_fma_f32 v[22:23], v[24:25], v[0:1], v[6:7] op_sel:[0,1,1] op_sel_hi:[1,1,0] neg_lo:[0,0,1] neg_hi:[0,0,1]
	v_pk_fma_f32 v[6:7], v[24:25], v[0:1], v[6:7] op_sel:[0,1,1] op_sel_hi:[1,1,0]
	s_nop 0
	v_cvt_pk_f16_f32 v5, v22, v7
	v_pk_mul_f32 v[6:7], v[82:83], v[10:11] op_sel_hi:[1,0]
	s_nop 0
	v_pk_fma_f32 v[22:23], v[82:83], v[2:3], v[6:7] op_sel:[0,0,1] op_sel_hi:[1,1,0] neg_lo:[0,0,1] neg_hi:[0,0,1]
	v_pk_fma_f32 v[6:7], v[82:83], v[2:3], v[6:7] op_sel:[0,0,1] op_sel_hi:[1,0,0]
	s_nop 0
	v_cvt_pk_f16_f32 v6, v22, v7
	v_mov_b32_e32 v22, v11
	v_pk_mul_f32 v[24:25], v[84:85], v[22:23] op_sel_hi:[1,0]
	s_nop 0
	v_pk_fma_f32 v[40:41], v[84:85], v[38:39], v[24:25] op_sel:[0,0,1] op_sel_hi:[1,0,0] neg_lo:[0,0,1] neg_hi:[0,0,1]
	v_pk_fma_f32 v[24:25], v[84:85], v[38:39], v[24:25] op_sel:[0,0,1] op_sel_hi:[1,0,0]
	s_nop 0
	v_cvt_pk_f16_f32 v7, v40, v25
	v_lshlrev_b64 v[24:25], 1, v[118:119]
	v_lshl_add_u64 v[40:41], s[10:11], 0, v[24:25]
	v_lshl_add_u64 v[40:41], v[40:41], 0, v[16:17]
	v_lshl_add_u64 v[40:41], v[40:41], 0, v[138:139]
	global_store_dwordx4 v[40:41], v[4:7], off sc1
	s_nop 1
	v_pk_mul_f32 v[4:5], v[30:31], v[8:9] op_sel_hi:[1,0]
	s_nop 0
	v_pk_fma_f32 v[6:7], v[30:31], v[0:1], v[4:5] op_sel:[0,0,1] op_sel_hi:[1,1,0] neg_lo:[0,0,1] neg_hi:[0,0,1]
	v_pk_fma_f32 v[4:5], v[30:31], v[0:1], v[4:5] op_sel:[0,0,1] op_sel_hi:[1,0,0]
	s_nop 0
	v_cvt_pk_f16_f32 v4, v6, v5
	v_pk_mul_f32 v[6:7], v[32:33], v[8:9] op_sel:[0,1]
	s_nop 0
	v_pk_fma_f32 v[8:9], v[32:33], v[0:1], v[6:7] op_sel:[0,1,1] op_sel_hi:[1,1,0] neg_lo:[0,0,1] neg_hi:[0,0,1]
	v_pk_fma_f32 v[0:1], v[32:33], v[0:1], v[6:7] op_sel:[0,1,1] op_sel_hi:[1,1,0]
	s_nop 0
	v_cvt_pk_f16_f32 v5, v8, v1
	v_pk_mul_f32 v[0:1], v[26:27], v[10:11] op_sel_hi:[1,0]
	s_nop 0
	v_pk_fma_f32 v[6:7], v[26:27], v[2:3], v[0:1] op_sel:[0,0,1] op_sel_hi:[1,1,0] neg_lo:[0,0,1] neg_hi:[0,0,1]
	v_pk_fma_f32 v[0:1], v[26:27], v[2:3], v[0:1] op_sel:[0,0,1] op_sel_hi:[1,0,0]
	s_nop 0
	v_cvt_pk_f16_f32 v6, v6, v1
	v_pk_mul_f32 v[0:1], v[28:29], v[22:23] op_sel_hi:[1,0]
	s_nop 0
	v_pk_fma_f32 v[2:3], v[28:29], v[38:39], v[0:1] op_sel:[0,0,1] op_sel_hi:[1,0,0] neg_lo:[0,0,1] neg_hi:[0,0,1]
	v_pk_fma_f32 v[0:1], v[28:29], v[38:39], v[0:1] op_sel:[0,0,1] op_sel_hi:[1,0,0]
	v_cvt_pk_f16_f32 v3, v48, v49
	v_cvt_pk_f16_f32 v7, v2, v1
	v_lshl_add_u64 v[0:1], s[12:13], 0, v[24:25]
	v_lshl_add_u64 v[0:1], v[0:1], 0, v[16:17]
	v_lshl_add_u64 v[0:1], v[0:1], 0, v[138:139]
	global_store_dwordx4 v[0:1], v[4:7], off sc1
	v_lshlrev_b64 v[0:1], 18, v[18:19]
	v_lshlrev_b32_e32 v2, 7, v145
	v_lshl_add_u64 v[0:1], s[14:15], 0, v[0:1]
	v_and_b32_e32 v16, 0x3e000, v2
	v_lshl_add_u64 v[0:1], v[0:1], 0, v[16:17]
	v_lshlrev_b32_e32 v16, 4, v20
	v_lshl_add_u64 v[4:5], v[0:1], 0, v[16:17]
	v_lshlrev_b32_e32 v16, 12, v144
	v_cvt_pk_f16_f32 v2, v46, v47
	v_cvt_pk_f16_f32 v1, v72, v73
	v_cvt_pk_f16_f32 v0, v70, v71
	v_lshl_add_u64 v[4:5], v[4:5], 0, v[16:17]
	global_store_dwordx4 v[4:5], v[0:3], off sc1
	s_nop 1
	v_cvt_pk_f16_f32 v3, v36, v37
	v_cvt_pk_f16_f32 v2, v34, v35
	v_cvt_pk_f16_f32 v1, v60, v61
	v_cvt_pk_f16_f32 v0, v58, v59
	global_store_dwordx4 v[4:5], v[0:3], off offset:1024 sc1
	s_nop 1
	v_cvt_pk_f16_f32 v3, v64, v65
	v_cvt_pk_f16_f32 v2, v62, v63
	v_cvt_pk_f16_f32 v1, v14, v15
	v_cvt_pk_f16_f32 v0, v12, v13
	global_store_dwordx4 v[4:5], v[0:3], off offset:2048 sc1
	s_nop 1
	v_cvt_pk_f16_f32 v3, v52, v53
	v_cvt_pk_f16_f32 v2, v50, v51
	v_cvt_pk_f16_f32 v1, v80, v81
	v_cvt_pk_f16_f32 v0, v78, v79
	global_store_dwordx4 v[4:5], v[0:3], off offset:3072 sc1
	s_endpgm
	.p2align	8

	.amdhsa_kernel _Z9gemm_gldsILi256ELi192ELi4ELi2ELi2ELi4ELi8ELi0ELi4096ELi3072ELi1024EEvPKDF16_S1_PfPKfS4_PKiPDF16_S7_S7_
		.amdhsa_group_segment_fixed_size 114688
		.amdhsa_private_segment_fixed_size 0
		.amdhsa_kernarg_size 72
		.amdhsa_user_sgpr_count 2
		.amdhsa_user_sgpr_dispatch_ptr 0
		.amdhsa_user_sgpr_queue_ptr 0
		.amdhsa_user_sgpr_kernarg_segment_ptr 1
		.amdhsa_user_sgpr_dispatch_id 0
		.amdhsa_user_sgpr_kernarg_preload_length 0
		.amdhsa_user_sgpr_kernarg_preload_offset 0
		.amdhsa_user_sgpr_private_segment_size 0
		.amdhsa_uses_dynamic_stack 0
		.amdhsa_enable_private_segment 0
		.amdhsa_system_sgpr_workgroup_id_x 1
		.amdhsa_system_sgpr_workgroup_id_y 0
		.amdhsa_system_sgpr_workgroup_id_z 0
		.amdhsa_system_sgpr_workgroup_info 0
		.amdhsa_system_vgpr_workitem_id 0
		.amdhsa_next_free_vgpr 217
		.amdhsa_next_free_sgpr 96
		.amdhsa_accum_offset 220
		.amdhsa_reserve_vcc 0
		.amdhsa_float_round_mode_32 0
		.amdhsa_float_round_mode_16_64 0
		.amdhsa_float_denorm_mode_32 3
		.amdhsa_float_denorm_mode_16_64 3
		.amdhsa_dx10_clamp 1
		.amdhsa_ieee_mode 1
		.amdhsa_fp16_overflow 0
		.amdhsa_tg_split 0
		.amdhsa_exception_fp_ieee_invalid_op 0
		.amdhsa_exception_fp_denorm_src 0
		.amdhsa_exception_fp_ieee_div_zero 0
		.amdhsa_exception_fp_ieee_overflow 0
		.amdhsa_exception_fp_ieee_underflow 0
		.amdhsa_exception_fp_ieee_inexact 0
		.amdhsa_exception_int_div_zero 0
	.end_amdhsa_kernel

amdhsa.kernels:
  - .agpr_count:     0
    .args:
      - .actual_access:  read_only
        .address_space:  global
        .offset:         0
        .size:           8
        .value_kind:     global_buffer
      - .actual_access:  read_only
        .address_space:  global
        .offset:         8
        .size:           8
        .value_kind:     global_buffer
      - .actual_access:  read_only
        .address_space:  global
        .offset:         16
        .size:           8
        .value_kind:     global_buffer
      - .actual_access:  read_only
        .address_space:  global
        .offset:         24
        .size:           8
        .value_kind:     global_buffer
      - .actual_access:  read_only
        .address_space:  global
        .offset:         32
        .size:           8
        .value_kind:     global_buffer
      - .actual_access:  read_only
        .address_space:  global
        .offset:         40
        .size:           8
        .value_kind:     global_buffer
      - .actual_access:  write_only
        .address_space:  global
        .offset:         48
        .size:           8
        .value_kind:     global_buffer
      - .actual_access:  write_only
        .address_space:  global
        .offset:         56
        .size:           8
        .value_kind:     global_buffer
      - .actual_access:  write_only
        .address_space:  global
        .offset:         64
        .size:           8
        .value_kind:     global_buffer
      - .actual_access:  write_only
        .address_space:  global
        .offset:         72
        .size:           8
        .value_kind:     global_buffer
      - .actual_access:  write_only
        .address_space:  global
        .offset:         80
        .size:           8
        .value_kind:     global_buffer
    .group_segment_fixed_size: 16640
    .kernarg_segment_align: 8
    .kernarg_segment_size: 88
    .language:       OpenCL C
    .language_version:
      - 2
      - 0
    .max_flat_workgroup_size: 256
    .name:           _Z11prep_kernelPKfS0_S0_S0_S0_PKiPDF16_S3_S3_PyPi
    .private_segment_fixed_size: 0
    .sgpr_count:     54
    .sgpr_spill_count: 0
    .symbol:         _Z11prep_kernelPKfS0_S0_S0_S0_PKiPDF16_S3_S3_PyPi.kd
    .uniform_work_group_size: 1
    .uses_dynamic_stack: false
    .vgpr_count:     46
    .vgpr_spill_count: 0
    .wavefront_size: 64
  - .agpr_count:     0
    .args:
      - .actual_access:  read_only
        .address_space:  global
        .offset:         0
        .size:           8
        .value_kind:     global_buffer
      - .actual_access:  read_only
        .address_space:  global
        .offset:         8
        .size:           8
        .value_kind:     global_buffer
      - .actual_access:  read_only
        .address_space:  global
        .offset:         16
        .size:           8
        .value_kind:     global_buffer
      - .actual_access:  read_only
        .address_space:  global
        .offset:         24
        .size:           8
        .value_kind:     global_buffer
      - .actual_access:  read_only
        .address_space:  global
        .offset:         32
        .size:           8
        .value_kind:     global_buffer
      - .actual_access:  write_only
        .address_space:  global
        .offset:         40
        .size:           8
        .value_kind:     global_buffer
    .group_segment_fixed_size: 36864
    .kernarg_segment_align: 8
    .kernarg_segment_size: 48
    .language:       OpenCL C
    .language_version:
      - 2
      - 0
    .max_flat_workgroup_size: 256
    .name:           _Z11attn_kernelPKDF16_S0_S0_PKyPKiPDF16_
    .private_segment_fixed_size: 0
    .sgpr_count:     32
    .sgpr_spill_count: 0
    .symbol:         _Z11attn_kernelPKDF16_S0_S0_PKyPKiPDF16_.kd
    .uniform_work_group_size: 1
    .uses_dynamic_stack: false
    .vgpr_count:     124
    .vgpr_spill_count: 0
    .wavefront_size: 64
  - .agpr_count:     0
    .args:
      - .address_space:  global
        .offset:         0
        .size:           8
        .value_kind:     global_buffer
      - .address_space:  global
        .offset:         8
        .size:           8
        .value_kind:     global_buffer
      - .actual_access:  read_only
        .address_space:  global
        .offset:         16
        .size:           8
        .value_kind:     global_buffer
      - .actual_access:  read_only
        .address_space:  global
        .offset:         24
        .size:           8
        .value_kind:     global_buffer
      - .actual_access:  read_only
        .address_space:  global
        .offset:         32
        .size:           8
        .value_kind:     global_buffer
      - .actual_access:  read_only
        .address_space:  global
        .offset:         40
        .size:           8
        .value_kind:     global_buffer
      - .actual_access:  write_only
        .address_space:  global
        .offset:         48
        .size:           8
        .value_kind:     global_buffer
      - .actual_access:  write_only
        .address_space:  global
        .offset:         56
        .size:           8
        .value_kind:     global_buffer
      - .actual_access:  write_only
        .address_space:  global
        .offset:         64
        .size:           8
        .value_kind:     global_buffer
    .group_segment_fixed_size: 114688
    .kernarg_segment_align: 8
    .kernarg_segment_size: 72
    .language:       OpenCL C
    .language_version:
      - 2
      - 0
    .max_flat_workgroup_size: 512
    .name:           _Z9gemm_gldsILi256ELi192ELi4ELi2ELi2ELi4ELi8ELi0ELi4096ELi3072ELi1024EEvPKDF16_S1_PfPKfS4_PKiPDF16_S7_S7_
    .private_segment_fixed_size: 0
    .sgpr_count:     29
    .sgpr_spill_count: 0
    .symbol:         _Z9gemm_gldsILi256ELi192ELi4ELi2ELi2ELi4ELi8ELi0ELi4096ELi3072ELi1024EEvPKDF16_S1_PfPKfS4_PKiPDF16_S7_S7_.kd
    .uniform_work_group_size: 1
    .uses_dynamic_stack: false
    .vgpr_count:     217
    .vgpr_spill_count: 0
    .wavefront_size: 64
  - .agpr_count:     0
    .args:
      - .address_space:  global
        .offset:         0
        .size:           8
        .value_kind:     global_buffer
      - .address_space:  global
        .offset:         8
        .size:           8
        .value_kind:     global_buffer
      - .actual_access:  write_only
        .address_space:  global
        .offset:         16
        .size:           8
        .value_kind:     global_buffer
      - .actual_access:  read_only
        .address_space:  global
        .offset:         24
        .size:           8
        .value_kind:     global_buffer
      - .actual_access:  read_only
        .address_space:  global
        .offset:         32
        .size:           8
        .value_kind:     global_buffer
      - .actual_access:  read_only
        .address_space:  global
        .offset:         40
        .size:           8
        .value_kind:     global_buffer
      - .actual_access:  read_only
        .address_space:  global
        .offset:         48
        .size:           8
        .value_kind:     global_buffer
      - .actual_access:  read_only
        .address_space:  global
        .offset:         56
        .size:           8
        .value_kind:     global_buffer
      - .actual_access:  read_only
        .address_space:  global
        .offset:         64
        .size:           8
        .value_kind:     global_buffer
    .group_segment_fixed_size: 98304
    .kernarg_segment_align: 8
    .kernarg_segment_size: 72
    .language:       OpenCL C
    .language_version:
      - 2
      - 0
    .max_flat_workgroup_size: 512
    .name:           _Z9gemm_gldsILi128ELi128ELi4ELi2ELi3ELi8ELi4ELi1ELi4096ELi1024ELi1024EEvPKDF16_S1_PfPKfS4_PKiPDF16_S7_S7_
    .private_segment_fixed_size: 0
    .sgpr_count:     20
    .sgpr_spill_count: 0
    .symbol:         _Z9gemm_gldsILi128ELi128ELi4ELi2ELi3ELi8ELi4ELi1ELi4096ELi1024ELi1024EEvPKDF16_S1_PfPKfS4_PKiPDF16_S7_S7_.kd
    .uniform_work_group_size: 1
    .uses_dynamic_stack: false
    .vgpr_count:     92
    .vgpr_spill_count: 0
    .wavefront_size: 64
